# scan loader: weight-tile store/load moved to the end of window A so tile loads get a full chunk period before they are waited on
# speedup vs baseline: 1.0069x; 1.0005x over previous
; __device__ __forceinline__ void p4_scan(const Args& a, const Frame& F) {
;     ...
;             auto conv_load = [&](int it) {
;                 const float* cW; int cN, cn;
;                 if (it < 32768) { const int e = it >> 10, sb = it & 1023; ck0 = (sb >> 6) * 64; cn = (sb & 63) * 32 + (lane & 31); cN = 2048; cW = a.in[IN_W1] + (size_t)e * 1024 * 2048; cD = (bf16*)(a.ws + WS_W1T);
;                     const int up = cn >= 1024, nn = cn & 1023; crow = e * 2048 + (nn >> 7) * 256 + up * 128 + (nn & 127); }
;                 else { const int it2 = it - 32768, e = it2 >> 9, sb = it2 & 511; ck0 = (sb >> 5) * 64; cn = (sb & 31) * 32 + (lane & 31); cN = 1024; cW = a.in[IN_W2] + (size_t)e * 1024 * 1024; cD = (bf16*)(a.ws + WS_W2T); crow = e * 1024 + cn; }
; #pragma unroll
;                 for (int i = 0; i < 32; ++i) cv[i] = cW[(size_t)(ck0 + (lane >> 5) + 2 * i) * cN + cn];
;             };
;     ...
;             conv_load(lw);
.LBB0_490:
	v_and_b32_e32 v82, 0x3c0, v9
	v_or_b32_e32 v14, v82, v158
	v_mov_b32_e32 v9, v145
	v_mul_u32_u24_e32 v12, s54, v14
	v_lshl_add_u64 v[8:9], v[8:9], 2, s[56:57]
	v_lshlrev_b32_e32 v12, 2, v12
	v_mov_b32_e32 v13, v145
	v_lshl_add_u64 v[12:13], v[8:9], 0, v[12:13]
	global_load_dword v148, v[12:13], off
	v_or_b32_e32 v12, 2, v14
	v_mul_u32_u24_e32 v12, s54, v12
	v_lshlrev_b32_e32 v12, 2, v12
	v_mov_b32_e32 v13, v145
	v_lshl_add_u64 v[12:13], v[8:9], 0, v[12:13]
	global_load_dword v141, v[12:13], off
	v_or_b32_e32 v12, 4, v14
	v_mul_u32_u24_e32 v12, s54, v12
	v_lshlrev_b32_e32 v12, 2, v12
	v_mov_b32_e32 v13, v145
	v_lshl_add_u64 v[12:13], v[8:9], 0, v[12:13]
	global_load_dword v149, v[12:13], off
	v_or_b32_e32 v12, 6, v14
	v_mul_u32_u24_e32 v12, s54, v12
	v_lshlrev_b32_e32 v12, 2, v12
	v_mov_b32_e32 v13, v145
	v_lshl_add_u64 v[12:13], v[8:9], 0, v[12:13]
	global_load_dword v137, v[12:13], off
	v_or_b32_e32 v12, 8, v14
	v_mul_u32_u24_e32 v12, s54, v12
	v_lshlrev_b32_e32 v12, 2, v12
	v_mov_b32_e32 v13, v145
	v_lshl_add_u64 v[12:13], v[8:9], 0, v[12:13]
	global_load_dword v142, v[12:13], off
	v_or_b32_e32 v12, 10, v14
	v_mul_u32_u24_e32 v12, s54, v12
	v_lshlrev_b32_e32 v12, 2, v12
	v_mov_b32_e32 v13, v145
	v_lshl_add_u64 v[12:13], v[8:9], 0, v[12:13]
	global_load_dword v81, v[12:13], off
	v_or_b32_e32 v12, 12, v14
	v_mul_u32_u24_e32 v12, s54, v12
	v_lshlrev_b32_e32 v12, 2, v12
	v_mov_b32_e32 v13, v145
	v_lshl_add_u64 v[12:13], v[8:9], 0, v[12:13]
	global_load_dword v138, v[12:13], off
	v_or_b32_e32 v12, 14, v14
	v_mul_u32_u24_e32 v12, s54, v12
	v_lshlrev_b32_e32 v12, 2, v12
	v_mov_b32_e32 v13, v145
	v_lshl_add_u64 v[12:13], v[8:9], 0, v[12:13]
	global_load_dword v151, v[12:13], off
	v_or_b32_e32 v12, 16, v14
	v_mul_u32_u24_e32 v12, s54, v12
	v_lshlrev_b32_e32 v12, 2, v12
	v_mov_b32_e32 v13, v145
	v_lshl_add_u64 v[12:13], v[8:9], 0, v[12:13]
	global_load_dword v152, v[12:13], off
	v_or_b32_e32 v12, 18, v14
	v_mul_u32_u24_e32 v12, s54, v12
	v_lshlrev_b32_e32 v12, 2, v12
	v_mov_b32_e32 v13, v145
	v_lshl_add_u64 v[12:13], v[8:9], 0, v[12:13]
	global_load_dword v143, v[12:13], off
	v_or_b32_e32 v12, 20, v14
	v_mul_u32_u24_e32 v12, s54, v12
	v_lshlrev_b32_e32 v12, 2, v12
	v_mov_b32_e32 v13, v145
	v_lshl_add_u64 v[12:13], v[8:9], 0, v[12:13]
	global_load_dword v150, v[12:13], off
	v_or_b32_e32 v12, 22, v14
	v_mul_u32_u24_e32 v12, s54, v12
	v_lshlrev_b32_e32 v12, 2, v12
	v_mov_b32_e32 v13, v145
	v_lshl_add_u64 v[12:13], v[8:9], 0, v[12:13]
	global_load_dword v139, v[12:13], off
	v_or_b32_e32 v12, 24, v14
	v_mul_u32_u24_e32 v12, s54, v12
	v_lshlrev_b32_e32 v12, 2, v12
	v_mov_b32_e32 v13, v145
	v_lshl_add_u64 v[12:13], v[8:9], 0, v[12:13]
	global_load_dword v147, v[12:13], off
	v_or_b32_e32 v12, 26, v14
	v_mul_u32_u24_e32 v12, s54, v12
	v_lshlrev_b32_e32 v12, 2, v12
	v_mov_b32_e32 v13, v145
	v_lshl_add_u64 v[12:13], v[8:9], 0, v[12:13]
	global_load_dword v83, v[12:13], off
	v_or_b32_e32 v12, 28, v14
	v_mul_u32_u24_e32 v12, s54, v12
	v_lshlrev_b32_e32 v12, 2, v12
	v_mov_b32_e32 v13, v145
	v_lshl_add_u64 v[12:13], v[8:9], 0, v[12:13]
	global_load_dword v140, v[12:13], off
	v_or_b32_e32 v12, 30, v14
	v_mul_u32_u24_e32 v12, s54, v12
	v_lshlrev_b32_e32 v12, 2, v12
	v_mov_b32_e32 v13, v145
	v_lshl_add_u64 v[12:13], v[8:9], 0, v[12:13]
	global_load_dword v153, v[12:13], off
	v_or_b32_e32 v12, 32, v14
	v_mul_u32_u24_e32 v12, s54, v12
	v_lshlrev_b32_e32 v12, 2, v12
	v_mov_b32_e32 v13, v145
	v_lshl_add_u64 v[12:13], v[8:9], 0, v[12:13]
	global_load_dword v183, v[12:13], off
	v_or_b32_e32 v12, 34, v14
	v_mul_u32_u24_e32 v12, s54, v12
	v_lshlrev_b32_e32 v12, 2, v12
	v_mov_b32_e32 v13, v145
	v_lshl_add_u64 v[12:13], v[8:9], 0, v[12:13]
	global_load_dword v179, v[12:13], off
	v_or_b32_e32 v12, 36, v14
	v_mul_u32_u24_e32 v12, s54, v12
	v_lshlrev_b32_e32 v12, 2, v12
	v_mov_b32_e32 v13, v145
	v_lshl_add_u64 v[12:13], v[8:9], 0, v[12:13]
	global_load_dword v184, v[12:13], off
	v_or_b32_e32 v12, 38, v14
	v_mul_u32_u24_e32 v12, s54, v12
	v_lshlrev_b32_e32 v12, 2, v12
	v_mov_b32_e32 v13, v145
	v_lshl_add_u64 v[12:13], v[8:9], 0, v[12:13]
	global_load_dword v175, v[12:13], off
	v_or_b32_e32 v12, 40, v14
	v_mul_u32_u24_e32 v12, s54, v12
	v_lshlrev_b32_e32 v12, 2, v12
	v_mov_b32_e32 v13, v145
	v_lshl_add_u64 v[12:13], v[8:9], 0, v[12:13]
	global_load_dword v180, v[12:13], off
	v_or_b32_e32 v12, 42, v14
	v_mul_u32_u24_e32 v12, s54, v12
	v_lshlrev_b32_e32 v12, 2, v12
	v_mov_b32_e32 v13, v145
	v_lshl_add_u64 v[12:13], v[8:9], 0, v[12:13]
	global_load_dword v173, v[12:13], off
	v_or_b32_e32 v12, 44, v14
	v_mul_u32_u24_e32 v12, s54, v12
	v_lshlrev_b32_e32 v12, 2, v12
	v_mov_b32_e32 v13, v145
	v_lshl_add_u64 v[12:13], v[8:9], 0, v[12:13]
	global_load_dword v176, v[12:13], off
	v_or_b32_e32 v12, 46, v14
	v_mul_u32_u24_e32 v12, s54, v12
	v_lshlrev_b32_e32 v12, 2, v12
	v_mov_b32_e32 v13, v145
	v_lshl_add_u64 v[12:13], v[8:9], 0, v[12:13]
	global_load_dword v186, v[12:13], off
	v_or_b32_e32 v12, 48, v14
	v_mul_u32_u24_e32 v12, s54, v12
	v_lshlrev_b32_e32 v12, 2, v12
	v_mov_b32_e32 v13, v145
	v_lshl_add_u64 v[12:13], v[8:9], 0, v[12:13]
	global_load_dword v187, v[12:13], off
	v_or_b32_e32 v12, 50, v14
	v_mul_u32_u24_e32 v12, s54, v12
	v_lshlrev_b32_e32 v12, 2, v12
	v_mov_b32_e32 v13, v145
	v_lshl_add_u64 v[12:13], v[8:9], 0, v[12:13]
	global_load_dword v181, v[12:13], off
	v_or_b32_e32 v12, 52, v14
; __device__ __forceinline__ void p4_scan(const Args& a, const Frame& F) {
;     ...
;             auto prefetch = [&](int ci) {
;                 const int base = chunk_base(ci);
; #pragma unroll
;                 for (int i = 0; i < 8; ++i) { const int p = ht + 256 * i, row = p >> 4, c16 = p & 15; const int tok = base + (dir ? 127 - row : row);
;                     pq[i] = *(const u32x4*)(QKC + (size_t)tok * 1024 + h * 128 + c16 * 8); pk[i] = *(const u32x4*)(QKC + (size_t)tok * 1024 + 512 + h * 128 + c16 * 8); }
; #pragma unroll
;                 for (int i = 0; i < 2; ++i) { const int p = ht + 256 * i, row = p >> 2, cc = p & 3; const int tok = base + (dir ? 127 - row : row);
;                     pv[i] = *(const u32x4*)(PV + (size_t)tok * 512 + h * 128 + vs * 32 + cc * 8); pga[i] = GS[(size_t)hd * TA + tok]; }
; #pragma unroll
;                 for (int i = 0; i < 2; ++i) { const int idx = ht + 256 * i; if (idx < 384) { const int row = idx & 127, arr = idx >> 7; const int tok = base + (dir ? 127 - row : row); pgl[i] = GS[(size_t)(arr * 8 + hd) * TA + tok]; } }
;                 pbt = CH[(hd * 528 + (base >> 7)) * 2]; ppx = CH[(hd * 528 + (base >> 7)) * 2 + 1];
;             };
;     ...
;             auto conv_load = [&](int it) {
;                 const float* cW; int cN, cn;
;                 if (it < 32768) { const int e = it >> 10, sb = it & 1023; ck0 = (sb >> 6) * 64; cn = (sb & 63) * 32 + (lane & 31); cN = 2048; cW = a.in[IN_W1] + (size_t)e * 1024 * 2048; cD = (bf16*)(a.ws + WS_W1T);
;                     const int up = cn >= 1024, nn = cn & 1023; crow = e * 2048 + (nn >> 7) * 256 + up * 128 + (nn & 127); }
;                 else { const int it2 = it - 32768, e = it2 >> 9, sb = it2 & 511; ck0 = (sb >> 5) * 64; cn = (sb & 31) * 32 + (lane & 31); cN = 1024; cW = a.in[IN_W2] + (size_t)e * 1024 * 1024; cD = (bf16*)(a.ws + WS_W2T); crow = e * 1024 + cn; }
; #pragma unroll
;                 for (int i = 0; i < 32; ++i) cv[i] = cW[(size_t)(ck0 + (lane >> 5) + 2 * i) * cN + cn];
;             };
	v_mul_u32_u24_e32 v12, s54, v12
	v_lshlrev_b32_e32 v12, 2, v12
	v_mov_b32_e32 v13, v145
	v_lshl_add_u64 v[12:13], v[8:9], 0, v[12:13]
	global_load_dword v185, v[12:13], off
	v_or_b32_e32 v12, 54, v14
	v_mul_u32_u24_e32 v12, s54, v12
	v_lshlrev_b32_e32 v12, 2, v12
	v_mov_b32_e32 v13, v145
	v_lshl_add_u64 v[12:13], v[8:9], 0, v[12:13]
	global_load_dword v177, v[12:13], off
	v_or_b32_e32 v12, 56, v14
	v_mul_u32_u24_e32 v12, s54, v12
	v_lshlrev_b32_e32 v12, 2, v12
	v_mov_b32_e32 v13, v145
	v_lshl_add_u64 v[12:13], v[8:9], 0, v[12:13]
	global_load_dword v182, v[12:13], off
	v_or_b32_e32 v12, 58, v14
	v_mul_u32_u24_e32 v12, s54, v12
	v_lshlrev_b32_e32 v12, 2, v12
	v_mov_b32_e32 v13, v145
	v_lshl_add_u64 v[12:13], v[8:9], 0, v[12:13]
	global_load_dword v174, v[12:13], off
	v_or_b32_e32 v12, 60, v14
	v_mul_u32_u24_e32 v12, s54, v12
	v_lshlrev_b32_e32 v12, 2, v12
	v_mov_b32_e32 v13, v145
	v_lshl_add_u64 v[12:13], v[8:9], 0, v[12:13]
	global_load_dword v178, v[12:13], off
	v_or_b32_e32 v12, 62, v14
	v_mul_u32_u24_e32 v12, s54, v12
	v_lshlrev_b32_e32 v12, 2, v12
	v_mov_b32_e32 v13, v145
	v_lshl_add_u64 v[8:9], v[8:9], 0, v[12:13]
	global_load_dword v188, v[8:9], off
	s_lshl_b32 s44, s44, 1
	s_add_u32 s54, s20, s44
	s_addc_u32 s55, s21, 0
	s_lshl_b32 s33, s33, 1
	s_add_u32 s54, s54, s33
	s_addc_u32 s55, s55, 0
	v_mov_b32_e32 v87, v145
	v_lshl_add_u64 v[86:87], s[54:55], 0, v[86:87]
	s_add_i32 s54, s34, s35
	v_mov_b64_e32 v[8:9], s[38:39]
	s_add_i32 s33, 0, 0x23430
	v_mad_i64_i32 v[88:89], s[34:35], v88, s95, v[8:9]
	v_mad_i64_i32 v[90:91], s[34:35], v90, s95, v[8:9]
	s_add_i32 s54, s54, 0x10000
	v_add_u32_e32 v12, s33, v11
	s_lshl_b32 s33, s58, 13
	s_xor_b32 s34, s54, 0x80
	s_add_u32 s54, s16, s44
	v_add_u32_e32 v11, s89, v11
	s_addc_u32 s55, s17, 0
	v_lshl_add_u64 v[92:93], s[54:55], 0, v[144:145]
	s_mov_b32 s44, 0
	v_mov_b32_e32 v136, 0
	v_add_u32_e32 v134, v12, v10
	v_add_u32_e32 v135, v11, v10
	v_add_u32_e32 v214, s34, v96
	v_ashrrev_i32_e32 v215, 31, v214
	v_lshlrev_b64 v[214:215], 11, v[214:215]
	v_lshl_add_u64 v[214:215], v[92:93], 0, v[214:215]
	global_load_dwordx4 v[220:223], v[214:215], off offset:1024
	v_add_u32_e32 v214, s34, v97
	v_ashrrev_i32_e32 v215, 31, v214
	v_lshlrev_b64 v[214:215], 11, v[214:215]
	v_lshl_add_u64 v[214:215], v[92:93], 0, v[214:215]
	global_load_dwordx4 v[224:227], v[214:215], off offset:1024
	v_add_u32_e32 v214, s34, v98
	v_ashrrev_i32_e32 v215, 31, v214
	v_lshlrev_b64 v[214:215], 11, v[214:215]
	v_lshl_add_u64 v[214:215], v[92:93], 0, v[214:215]
	global_load_dwordx4 v[228:231], v[214:215], off offset:1024
	v_add_u32_e32 v214, s34, v99
	v_ashrrev_i32_e32 v215, 31, v214
	v_lshlrev_b64 v[214:215], 11, v[214:215]
	v_lshl_add_u64 v[214:215], v[92:93], 0, v[214:215]
	global_load_dwordx4 v[232:235], v[214:215], off offset:1024
	v_add_u32_e32 v214, s34, v100
	v_ashrrev_i32_e32 v215, 31, v214
	v_lshlrev_b64 v[214:215], 11, v[214:215]
	v_lshl_add_u64 v[214:215], v[92:93], 0, v[214:215]
	global_load_dwordx4 v[236:239], v[214:215], off offset:1024
	v_add_u32_e32 v214, s34, v101
	v_ashrrev_i32_e32 v215, 31, v214
	v_lshlrev_b64 v[214:215], 11, v[214:215]
	v_lshl_add_u64 v[214:215], v[92:93], 0, v[214:215]
	global_load_dwordx4 v[240:243], v[214:215], off offset:1024
	v_add_u32_e32 v214, s34, v102
	v_ashrrev_i32_e32 v215, 31, v214
	v_lshlrev_b64 v[214:215], 11, v[214:215]
	v_lshl_add_u64 v[214:215], v[92:93], 0, v[214:215]
	global_load_dwordx4 v[244:247], v[214:215], off offset:1024
	v_add_u32_e32 v214, s34, v103
	v_ashrrev_i32_e32 v215, 31, v214
	v_lshlrev_b64 v[214:215], 11, v[214:215]
	v_lshl_add_u64 v[214:215], v[92:93], 0, v[214:215]
	global_load_dwordx4 v[248:251], v[214:215], off offset:1024
	v_add_u32_e32 v214, s34, v96
	v_ashrrev_i32_e32 v215, 31, v214
	v_lshlrev_b64 v[214:215], 11, v[214:215]
	v_lshl_add_u64 v[214:215], v[92:93], 0, v[214:215]
	global_load_dwordx4 v[16:19], v[214:215], off
	v_add_u32_e32 v214, s34, v97
	v_ashrrev_i32_e32 v215, 31, v214
	v_lshlrev_b64 v[214:215], 11, v[214:215]
	v_lshl_add_u64 v[214:215], v[92:93], 0, v[214:215]
	global_load_dwordx4 v[20:23], v[214:215], off
	v_add_u32_e32 v214, s34, v98
	v_ashrrev_i32_e32 v215, 31, v214
	v_lshlrev_b64 v[214:215], 11, v[214:215]
	v_lshl_add_u64 v[214:215], v[92:93], 0, v[214:215]
	global_load_dwordx4 v[24:27], v[214:215], off
	v_add_u32_e32 v214, s34, v99
	v_ashrrev_i32_e32 v215, 31, v214
	v_lshlrev_b64 v[214:215], 11, v[214:215]
	v_lshl_add_u64 v[214:215], v[92:93], 0, v[214:215]
	global_load_dwordx4 v[28:31], v[214:215], off
	v_add_u32_e32 v214, s34, v100
	v_ashrrev_i32_e32 v215, 31, v214
	v_lshlrev_b64 v[214:215], 11, v[214:215]
	v_lshl_add_u64 v[214:215], v[92:93], 0, v[214:215]
	global_load_dwordx4 v[32:35], v[214:215], off
	v_add_u32_e32 v214, s34, v101
	v_ashrrev_i32_e32 v215, 31, v214
	v_lshlrev_b64 v[214:215], 11, v[214:215]
	v_lshl_add_u64 v[214:215], v[92:93], 0, v[214:215]
	global_load_dwordx4 v[36:39], v[214:215], off
	v_add_u32_e32 v214, s34, v102
	v_ashrrev_i32_e32 v215, 31, v214
	v_lshlrev_b64 v[214:215], 11, v[214:215]
	v_lshl_add_u64 v[214:215], v[92:93], 0, v[214:215]
	global_load_dwordx4 v[40:43], v[214:215], off
	v_add_u32_e32 v214, s34, v103
	v_ashrrev_i32_e32 v215, 31, v214
	v_lshlrev_b64 v[214:215], 11, v[214:215]
	v_lshl_add_u64 v[214:215], v[92:93], 0, v[214:215]
	global_load_dwordx4 v[44:47], v[214:215], off
	s_waitcnt vmcnt(8)
	s_branch .LBB0_492

; __device__ __forceinline__ void p4_scan(const Args& a, const Frame& F) {
;     ...
;             auto prefetch = [&](int ci) {
;                 const int base = chunk_base(ci);
; #pragma unroll
;                 for (int i = 0; i < 8; ++i) { const int p = ht + 256 * i, row = p >> 4, c16 = p & 15; const int tok = base + (dir ? 127 - row : row);
;                     pq[i] = *(const u32x4*)(QKC + (size_t)tok * 1024 + h * 128 + c16 * 8); pk[i] = *(const u32x4*)(QKC + (size_t)tok * 1024 + 512 + h * 128 + c16 * 8); }
; #pragma unroll
;                 for (int i = 0; i < 2; ++i) { const int p = ht + 256 * i, row = p >> 2, cc = p & 3; const int tok = base + (dir ? 127 - row : row);
;                     pv[i] = *(const u32x4*)(PV + (size_t)tok * 512 + h * 128 + vs * 32 + cc * 8); pga[i] = GS[(size_t)hd * TA + tok]; }
; #pragma unroll
;                 for (int i = 0; i < 2; ++i) { const int idx = ht + 256 * i; if (idx < 384) { const int row = idx & 127, arr = idx >> 7; const int tok = base + (dir ? 127 - row : row); pgl[i] = GS[(size_t)(arr * 8 + hd) * TA + tok]; } }
.LBB0_492:
	s_waitcnt vmcnt(40)
	s_add_i32 s35, s44, 1
	s_cmpk_eq_i32 s44, 0x41
	s_cselect_b32 s56, s44, s35
	s_sub_i32 s58, 0x41, s56
	v_sub_co_u32_e64 v8, s[54:55], s56, 2
	s_and_b64 s[56:57], s[4:5], exec
	v_readfirstlane_b32 s56, v8
	s_cselect_b32 s56, s56, s58
	s_lshl_b32 s56, s56, 7
	s_add_i32 s56, s56, s33
	s_and_b64 s[54:55], s[54:55], exec
	s_cselect_b32 s56, s34, s56
	v_add_u32_e32 v8, s56, v104
	v_ashrrev_i32_e32 v9, 31, v8
	v_lshlrev_b64 v[10:11], 10, v[8:9]
	v_lshl_add_u64 v[10:11], v[86:87], 0, v[10:11]
	v_lshl_add_u64 v[8:9], v[8:9], 2, s[50:51]
	global_load_dwordx4 v[12:15], v[10:11], off
	global_load_dword v172, v[8:9], off
	v_add_u32_e32 v8, s56, v105
	v_ashrrev_i32_e32 v9, 31, v8
	v_lshlrev_b64 v[10:11], 10, v[8:9]
	v_lshl_add_u64 v[10:11], v[86:87], 0, v[10:11]
	v_lshl_add_u64 v[94:95], v[8:9], 2, s[50:51]
	global_load_dwordx4 v[8:11], v[10:11], off
	s_nop 0
	global_load_dword v171, v[94:95], off
	v_or_b32_e32 v94, s56, v106
	v_ashrrev_i32_e32 v95, 31, v94
	s_and_saveexec_b64 s[54:55], s[6:7]
	s_cbranch_execz .LBB0_494
	v_lshl_add_u64 v[190:191], v[94:95], 2, v[88:89]
	global_load_dword v108, v[190:191], off

; #define LAS __attribute__((address_space(3)))
; __device__ __forceinline__ unsigned cvt_pk_bf16(float lo, float hi) { unsigned r; asm volatile("v_cvt_pk_bf16_f32 %0, %1, %2" : "=v"(r) : "v"(lo), "v"(hi)); return r; }
; __device__ __forceinline__ void p4_scan(const Args& a, const Frame& F) {
;     ...
;                 pbt = CH[(hd * 528 + (base >> 7)) * 2]; ppx = CH[(hd * 528 + (base >> 7)) * 2 + 1];
;             };
;             auto commitK = [&](int kbuf) {
; #pragma unroll
;                 for (int i = 0; i < 8; ++i) { const int p = ht + 256 * i, row = p >> 4, c16 = p & 15; *(LAS u32x4*)(L + kbuf + row * SP + c16 * 16) = pk[i]; } };
;     ...
;             auto conv_store = [&]() {
;                 const bool hi = lane >= 32;
;                 u32x4 o[4];
; #pragma unroll
;                 for (int i = 0; i < 16; ++i) { const float snd = hi ? cv[i] : cv[16 + i]; const float rcv = __shfl_xor(snd, 32);
;                     const unsigned pkd = pg8::cvt_pk_bf16(hi ? rcv : cv[i], hi ? cv[16 + i] : rcv);
;                     if ((i & 3) == 0) o[i >> 2].x = pkd; else if ((i & 3) == 1) o[i >> 2].y = pkd; else if ((i & 3) == 2) o[i >> 2].z = pkd; else o[i >> 2].w = pkd; }
;                 u32x4* dst = (u32x4*)(cD + (size_t)crow * 1024 + ck0 + (hi ? 32 : 0));
; #pragma unroll
;                 for (int j2 = 0; j2 < 4; ++j2) dst[j2] = o[j2];
;             };
.LBB0_496:
	s_or_b64 exec, exec, s[54:55]
	s_ashr_i32 s54, s56, 7
	s_add_i32 s54, s54, s76
	s_lshl_b32 s54, s54, 1
	s_ashr_i32 s55, s54, 31
	s_lshl_b64 s[54:55], s[54:55], 2
	s_add_u32 s54, s60, s54
	s_addc_u32 s55, s61, s55
	global_load_dwordx2 v[94:95], v145, s[54:55]
	s_bitcmp0_b32 s44, 0
	s_cselect_b64 s[54:55], -1, 0
	s_and_b64 s[56:57], s[54:55], exec
	s_cselect_b32 s56, 0x11000, s91
	s_add_i32 s56, s56, 0
	v_add3_u32 v144, s56, v109, v117
	ds_write_b128 v144, v[220:223]
	v_add3_u32 v48, s56, v110, v117
	ds_write_b128 v48, v[224:227]
	v_add3_u32 v48, s56, v111, v117
	ds_write_b128 v48, v[228:231]
	v_add3_u32 v48, s56, v112, v117
	ds_write_b128 v48, v[232:235]
	v_add3_u32 v48, s56, v113, v117
	ds_write_b128 v48, v[236:239]
	v_add3_u32 v48, s56, v114, v117
	ds_write_b128 v48, v[240:243]
	v_add3_u32 v48, s56, v115, v117
	ds_write_b128 v48, v[244:247]
	v_add3_u32 v48, s56, v116, v117
	ds_write_b128 v48, v[248:251]
	s_add_i32 s98, s35, 1
	s_min_i32 s98, s98, 0x41
	s_sub_i32 s99, 0x41, s98
	s_add_i32 s98, s98, -2
	s_and_b64 s[100:101], s[4:5], exec
	s_cselect_b32 s98, s98, s99
	s_lshl_b32 s98, s98, 7
	s_add_i32 s98, s98, s33
	v_add_u32_e32 v214, s98, v96
	v_ashrrev_i32_e32 v215, 31, v214
	v_lshlrev_b64 v[214:215], 11, v[214:215]
	v_lshl_add_u64 v[214:215], v[92:93], 0, v[214:215]
	global_load_dwordx4 v[220:223], v[214:215], off offset:1024
	v_add_u32_e32 v214, s98, v97
	v_ashrrev_i32_e32 v215, 31, v214
	v_lshlrev_b64 v[214:215], 11, v[214:215]
	v_lshl_add_u64 v[214:215], v[92:93], 0, v[214:215]
	global_load_dwordx4 v[224:227], v[214:215], off offset:1024
	v_add_u32_e32 v214, s98, v98
	v_ashrrev_i32_e32 v215, 31, v214
	v_lshlrev_b64 v[214:215], 11, v[214:215]
	v_lshl_add_u64 v[214:215], v[92:93], 0, v[214:215]
	global_load_dwordx4 v[228:231], v[214:215], off offset:1024
	v_add_u32_e32 v214, s98, v99
	v_ashrrev_i32_e32 v215, 31, v214
	v_lshlrev_b64 v[214:215], 11, v[214:215]
	v_lshl_add_u64 v[214:215], v[92:93], 0, v[214:215]
	global_load_dwordx4 v[232:235], v[214:215], off offset:1024
	v_add_u32_e32 v214, s98, v100
	v_ashrrev_i32_e32 v215, 31, v214
	v_lshlrev_b64 v[214:215], 11, v[214:215]
	v_lshl_add_u64 v[214:215], v[92:93], 0, v[214:215]
	global_load_dwordx4 v[236:239], v[214:215], off offset:1024
	v_add_u32_e32 v214, s98, v101
	v_ashrrev_i32_e32 v215, 31, v214
	v_lshlrev_b64 v[214:215], 11, v[214:215]
	v_lshl_add_u64 v[214:215], v[92:93], 0, v[214:215]
	global_load_dwordx4 v[240:243], v[214:215], off offset:1024
	v_add_u32_e32 v214, s98, v102
	v_ashrrev_i32_e32 v215, 31, v214
	v_lshlrev_b64 v[214:215], 11, v[214:215]
	v_lshl_add_u64 v[214:215], v[92:93], 0, v[214:215]
	global_load_dwordx4 v[244:247], v[214:215], off offset:1024
	v_add_u32_e32 v214, s98, v103
	v_ashrrev_i32_e32 v215, 31, v214
	v_lshlrev_b64 v[214:215], 11, v[214:215]
	v_lshl_add_u64 v[214:215], v[92:93], 0, v[214:215]
	global_load_dwordx4 v[248:251], v[214:215], off offset:1024
	s_waitcnt vmcnt(21)
	s_cmp_gt_u32 s44, 47
	s_cbranch_scc1 .LBB0_498
	v_permlane32_swap_b32_e32 v148, v183
	v_cvt_pk_bf16_f32 v48, v148, v183
	v_permlane32_swap_b32_e32 v141, v179
	v_cvt_pk_bf16_f32 v49, v141, v179
	v_permlane32_swap_b32_e32 v149, v184
	v_cvt_pk_bf16_f32 v50, v149, v184
	v_permlane32_swap_b32_e32 v137, v175
	v_cvt_pk_bf16_f32 v51, v137, v175
	v_permlane32_swap_b32_e32 v142, v180
	v_cvt_pk_bf16_f32 v52, v142, v180
	v_permlane32_swap_b32_e32 v81, v173
	v_cvt_pk_bf16_f32 v53, v81, v173
	v_permlane32_swap_b32_e32 v138, v176
	v_ashrrev_i32_e32 v81, 31, v80
	v_cvt_pk_bf16_f32 v54, v138, v176
	v_permlane32_swap_b32_e32 v151, v186
	v_cvt_pk_bf16_f32 v55, v151, v186
	v_permlane32_swap_b32_e32 v152, v187
	v_cvt_pk_bf16_f32 v56, v152, v187
	v_permlane32_swap_b32_e32 v143, v181
	v_cvt_pk_bf16_f32 v57, v143, v181
	v_permlane32_swap_b32_e32 v150, v185
	v_cvt_pk_bf16_f32 v58, v150, v185
	v_permlane32_swap_b32_e32 v139, v177
	v_cvt_pk_bf16_f32 v59, v139, v177
	v_permlane32_swap_b32_e32 v147, v182
	v_cvt_pk_bf16_f32 v60, v147, v182
	v_permlane32_swap_b32_e32 v83, v174
	v_mov_b32_e32 v147, v145
	v_cvt_pk_bf16_f32 v61, v83, v174
	v_permlane32_swap_b32_e32 v140, v178
	v_mov_b32_e32 v83, v145
	v_cvt_pk_bf16_f32 v62, v140, v178
	v_permlane32_swap_b32_e32 v153, v188
	v_cvt_pk_bf16_f32 v63, v153, v188
	v_lshlrev_b64 v[64:65], 11, v[80:81]
	v_lshl_add_u64 v[64:65], s[52:53], 0, v[64:65]
	v_lshl_add_u64 v[64:65], v[82:83], 1, v[64:65]
	v_lshl_add_u64 v[64:65], v[64:65], 0, v[146:147]
	global_store_dwordx4 v[64:65], v[48:51], off
	global_store_dwordx4 v[64:65], v[52:55], off offset:16
	global_store_dwordx4 v[64:65], v[56:59], off offset:32
	global_store_dwordx4 v[64:65], v[60:63], off offset:48
